# grid barrier: member workgroups poll the top generation word directly (one hop less); XCD generation bump removed in the 10 in-loop instances
# speedup vs baseline: 1.0018x; 1.0018x over previous
.LBB0_385:
	s_or_b64 exec, exec, s[2:3]
	v_cvt_f32_u32_e32 v4, v2
	s_waitcnt vmcnt(0)
	v_readfirstlane_b32 s2, v3
	v_sub_u32_e32 v3, 0, v2
	v_rcp_iflag_f32_e32 v4, v4
	v_add_u32_e32 v5, s2, v1
	v_mul_f32_e32 v4, 0x4f7ffffe, v4
	v_cvt_u32_f32_e32 v4, v4
	v_mul_lo_u32 v1, v3, v4
	v_mul_hi_u32 v1, v4, v1
	v_add_u32_e32 v1, v4, v1
	v_mul_hi_u32 v1, v5, v1
	v_mul_lo_u32 v3, v1, v2
	v_sub_u32_e32 v3, v5, v3
	v_add_u32_e32 v4, 1, v1
	v_cmp_ge_u32_e32 vcc, v3, v2
	s_nop 1
	v_cndmask_b32_e32 v1, v1, v4, vcc
	v_sub_u32_e32 v4, v3, v2
	v_cndmask_b32_e32 v3, v3, v4, vcc
	v_add_u32_e32 v4, 1, v1
	v_cmp_ge_u32_e32 vcc, v3, v2
	v_add_u32_e32 v3, 1, v5
	s_nop 0
	v_cndmask_b32_e32 v1, v1, v4, vcc
	v_mul_lo_u32 v4, v2, v1
	v_add_u32_e32 v2, v4, v2
	v_cmp_ne_u32_e32 vcc, v3, v2
	s_and_saveexec_b64 s[2:3], vcc
	s_xor_b64 s[2:3], exec, s[2:3]
	s_cbranch_execz .LBB0_399
	v_readlane_b32 s4, v254, 40
	v_readlane_b32 s5, v254, 41
	s_waitcnt lgkmcnt(0)
	s_nop 3
	global_load_dword v0, v113, s[4:5] sc1
	s_waitcnt vmcnt(0)
	v_cmp_eq_u32_e32 vcc, v0, v1
	s_and_saveexec_b64 s[4:5], vcc
	s_cbranch_execz .LBB0_398
	s_mov_b32 s17, 1
	s_mov_b64 s[6:7], 0
	s_branch .LBB0_389

.LBB0_391:
	v_readlane_b32 s10, v254, 40
	v_readlane_b32 s11, v254, 41
	s_add_i32 s17, s17, 1
	s_mov_b64 s[12:13], -1
	s_nop 2
	global_load_dword v0, v113, s[10:11] sc1
	s_waitcnt vmcnt(0)
	v_cmp_ne_u32_e32 vcc, v0, v1
	s_orn2_b64 s[10:11], vcc, exec
	s_branch .LBB0_388

.LBB0_416:
	s_or_b64 exec, exec, s[2:3]
	s_mov_b64 s[2:3], exec
	v_mbcnt_lo_u32_b32 v0, s2, 0
	v_mbcnt_hi_u32_b32 v0, s3, v0
	v_cmp_eq_u32_e32 vcc, 0, v0
	s_waitcnt vmcnt(0)
	buffer_inv sc1
	s_and_saveexec_b64 s[4:5], vcc
	s_cbranch_execz .LBB0_418
	s_bcnt1_i32_b64 s2, s[2:3]
	v_mov_b32_e32 v0, s2
	v_readlane_b32 s2, v254, 36
	v_readlane_b32 s3, v254, 37
	s_nop 4
.LBB0_418:
	s_or_b64 exec, exec, s[4:5]
	s_waitcnt vmcnt(0)

.LBB0_487:
	s_or_b64 exec, exec, s[2:3]
	s_mov_b64 s[2:3], exec
	v_mbcnt_lo_u32_b32 v0, s2, 0
	v_mbcnt_hi_u32_b32 v0, s3, v0
	v_cmp_eq_u32_e32 vcc, 0, v0
	s_waitcnt vmcnt(0)
	buffer_inv sc1
	s_and_saveexec_b64 s[4:5], vcc
	s_cbranch_execz .LBB0_489
	s_bcnt1_i32_b64 s2, s[2:3]
	v_mov_b32_e32 v0, s2
	v_readlane_b32 s2, v254, 36
	v_readlane_b32 s3, v254, 37
	s_nop 4
.LBB0_489:
	s_or_b64 exec, exec, s[4:5]
	s_waitcnt vmcnt(0)

.LBB0_532:
	s_or_b64 exec, exec, s[2:3]
	v_cvt_f32_u32_e32 v4, v2
	s_waitcnt vmcnt(0)
	v_readfirstlane_b32 s2, v3
	v_sub_u32_e32 v3, 0, v2
	v_rcp_iflag_f32_e32 v4, v4
	v_add_u32_e32 v5, s2, v1
	v_mul_f32_e32 v4, 0x4f7ffffe, v4
	v_cvt_u32_f32_e32 v4, v4
	v_mul_lo_u32 v1, v3, v4
	v_mul_hi_u32 v1, v4, v1
	v_add_u32_e32 v1, v4, v1
	v_mul_hi_u32 v1, v5, v1
	v_mul_lo_u32 v3, v1, v2
	v_sub_u32_e32 v3, v5, v3
	v_add_u32_e32 v4, 1, v1
	v_cmp_ge_u32_e32 vcc, v3, v2
	s_nop 1
	v_cndmask_b32_e32 v1, v1, v4, vcc
	v_sub_u32_e32 v4, v3, v2
	v_cndmask_b32_e32 v3, v3, v4, vcc
	v_add_u32_e32 v4, 1, v1
	v_cmp_ge_u32_e32 vcc, v3, v2
	v_add_u32_e32 v3, 1, v5
	s_nop 0
	v_cndmask_b32_e32 v1, v1, v4, vcc
	v_mul_lo_u32 v4, v2, v1
	v_add_u32_e32 v2, v4, v2
	v_cmp_ne_u32_e32 vcc, v3, v2
	s_and_saveexec_b64 s[2:3], vcc
	s_xor_b64 s[2:3], exec, s[2:3]
	s_cbranch_execz .LBB0_546
	v_readlane_b32 s4, v254, 40
	v_readlane_b32 s5, v254, 41
	s_waitcnt lgkmcnt(0)
	s_nop 3
	global_load_dword v0, v113, s[4:5] sc1
	s_waitcnt vmcnt(0)
	v_cmp_eq_u32_e32 vcc, v0, v1
	s_and_saveexec_b64 s[4:5], vcc
	s_cbranch_execz .LBB0_545
	s_mov_b32 s16, 1
	s_mov_b64 s[6:7], 0
	s_branch .LBB0_536

.LBB0_538:
	v_readlane_b32 s10, v254, 40
	v_readlane_b32 s11, v254, 41
	s_add_i32 s16, s16, 1
	s_mov_b64 s[12:13], -1
	s_nop 2
	global_load_dword v0, v113, s[10:11] sc1
	s_waitcnt vmcnt(0)
	v_cmp_ne_u32_e32 vcc, v0, v1
	s_orn2_b64 s[10:11], vcc, exec
	s_branch .LBB0_535

.LBB0_563:
	s_or_b64 exec, exec, s[2:3]
	s_mov_b64 s[2:3], exec
	v_mbcnt_lo_u32_b32 v0, s2, 0
	v_mbcnt_hi_u32_b32 v0, s3, v0
	v_cmp_eq_u32_e32 vcc, 0, v0
	s_waitcnt vmcnt(0)
	buffer_inv sc1
	s_and_saveexec_b64 s[4:5], vcc
	s_cbranch_execz .LBB0_565
	s_bcnt1_i32_b64 s2, s[2:3]
	v_mov_b32_e32 v0, s2
	v_readlane_b32 s2, v254, 36
	v_readlane_b32 s3, v254, 37
	s_nop 4
.LBB0_565:
	s_or_b64 exec, exec, s[4:5]
	s_waitcnt vmcnt(0)

.LBB0_747:
	s_or_b64 exec, exec, s[2:3]
	s_mov_b64 s[2:3], exec
	v_mbcnt_lo_u32_b32 v0, s2, 0
	v_mbcnt_hi_u32_b32 v0, s3, v0
	v_cmp_eq_u32_e32 vcc, 0, v0
	s_waitcnt vmcnt(0)
	buffer_inv sc1
	s_and_saveexec_b64 s[4:5], vcc
	s_cbranch_execz .LBB0_749
	s_bcnt1_i32_b64 s2, s[2:3]
	v_mov_b32_e32 v0, s2
	v_readlane_b32 s2, v254, 36
	v_readlane_b32 s3, v254, 37
	s_nop 4
.LBB0_749:
	s_or_b64 exec, exec, s[4:5]
	s_waitcnt vmcnt(0)

.LBB0_920:
	s_or_b64 exec, exec, s[2:3]
	s_mov_b64 s[2:3], exec
	v_mbcnt_lo_u32_b32 v0, s2, 0
	v_mbcnt_hi_u32_b32 v0, s3, v0
	v_cmp_eq_u32_e32 vcc, 0, v0
	s_waitcnt vmcnt(0)
	buffer_inv sc1
	s_and_saveexec_b64 s[4:5], vcc
	s_cbranch_execz .LBB0_922
	s_bcnt1_i32_b64 s2, s[2:3]
	v_mov_b32_e32 v0, s2
	v_readlane_b32 s2, v254, 36
	v_readlane_b32 s3, v254, 37
	s_nop 4
.LBB0_922:
	s_or_b64 exec, exec, s[4:5]
	s_waitcnt vmcnt(0)

.LBB0_1213:
	s_or_b64 exec, exec, s[2:3]
	s_mov_b64 s[2:3], exec
	v_mbcnt_lo_u32_b32 v0, s2, 0
	v_mbcnt_hi_u32_b32 v0, s3, v0
	v_cmp_eq_u32_e32 vcc, 0, v0
	s_waitcnt vmcnt(0)
	buffer_inv sc1
	s_and_saveexec_b64 s[4:5], vcc
	s_cbranch_execz .LBB0_1215
	s_bcnt1_i32_b64 s2, s[2:3]
	v_mov_b32_e32 v0, s2
	v_readlane_b32 s2, v254, 36
	v_readlane_b32 s3, v254, 37
	s_nop 4
.LBB0_1215:
	s_or_b64 exec, exec, s[4:5]
	s_waitcnt vmcnt(0)

.LBB0_1352:
	s_or_b64 exec, exec, s[2:3]
	s_mov_b64 s[2:3], exec
	v_mbcnt_lo_u32_b32 v0, s2, 0
	v_mbcnt_hi_u32_b32 v0, s3, v0
	v_cmp_eq_u32_e32 vcc, 0, v0
	s_waitcnt vmcnt(0)
	buffer_inv sc1
	s_and_saveexec_b64 s[4:5], vcc
	s_cbranch_execz .LBB0_1354
	s_bcnt1_i32_b64 s2, s[2:3]
	v_mov_b32_e32 v0, s2
	v_readlane_b32 s2, v254, 36
	v_readlane_b32 s3, v254, 37
	s_nop 4
.LBB0_1354:
	s_or_b64 exec, exec, s[4:5]
	s_waitcnt vmcnt(0)

.LBB0_1567:
	s_or_b64 exec, exec, s[2:3]
	s_mov_b64 s[2:3], exec
	v_mbcnt_lo_u32_b32 v0, s2, 0
	v_mbcnt_hi_u32_b32 v0, s3, v0
	v_cmp_eq_u32_e32 vcc, 0, v0
	s_waitcnt vmcnt(0)
	buffer_inv sc1
	s_and_saveexec_b64 s[4:5], vcc
	s_cbranch_execz .LBB0_1569
	s_bcnt1_i32_b64 s2, s[2:3]
	v_mov_b32_e32 v0, s2
	v_readlane_b32 s2, v254, 36
	v_readlane_b32 s3, v254, 37
	s_nop 4
.LBB0_1569:
	s_or_b64 exec, exec, s[4:5]
	s_waitcnt vmcnt(0)

.LBB0_1645:
	s_or_b64 exec, exec, s[2:3]
	s_mov_b64 s[2:3], exec
	v_mbcnt_lo_u32_b32 v0, s2, 0
	v_mbcnt_hi_u32_b32 v0, s3, v0
	v_cmp_eq_u32_e32 vcc, 0, v0
	s_waitcnt vmcnt(0)
	buffer_inv sc1
	s_and_saveexec_b64 s[4:5], vcc
	s_cbranch_execz .LBB0_1647
	s_bcnt1_i32_b64 s2, s[2:3]
	v_mov_b32_e32 v0, s2
	v_readlane_b32 s2, v254, 36
	v_readlane_b32 s3, v254, 37
	s_nop 4
.LBB0_1647:
	s_or_b64 exec, exec, s[4:5]
	s_waitcnt vmcnt(0)

.LBB0_1811:
	s_bcnt1_i32_b64 s2, s[2:3]
	v_mov_b32_e32 v0, s2
	v_readlane_b32 s2, v254, 36
	v_readlane_b32 s3, v254, 37
	s_nop 4
	s_getpc_b64 s[98:99]
